# passCU: h tile for the U1 epilogue prefetched during the last edge tile
# speedup vs baseline: 1.0902x; 1.0042x over previous
.LBB8_2:
	s_or_b64 exec, exec, s[20:21]
	s_waitcnt lgkmcnt(0)
	s_barrier
	s_load_dword s4, s[0:1], 0xb0
	v_and_b32_e32 v98, 31, v0
	v_lshlrev_b32_e32 v1, 3, v98
	s_lshr_b32 s3, s3, 6
	v_add_u32_e32 v1, 0xd000, v1
	ds_read2_b64 v[66:69], v1 offset0:96 offset1:128
	s_waitcnt lgkmcnt(0)
	s_mul_i32 s4, s4, s3
	s_add_i32 s4, s4, s2
	s_lshl_b32 s14, s4, 5
	s_cmpk_lt_i32 s4, 0xc35
	s_cselect_b64 s[16:17], -1, 0
	s_cmpk_gt_i32 s4, 0xc34
	s_mov_b32 s20, 0
	s_mov_b32 s37, 0
	s_cbranch_scc1 .LBB8_4
	s_mov_b32 s20, s62
	s_mov_b32 s28, s64
.LBB8_4:
	s_load_dwordx2 s[12:13], s[0:1], 0xa8
	s_load_dwordx2 s[18:19], s[0:1], 0x98
	s_waitcnt lgkmcnt(0)
	s_sub_i32 s4, s28, s20
	s_add_i32 s4, s4, 31
	v_and_b32_e32 v1, 63, v0
	s_ashr_i32 s15, s4, 5
	s_cmp_lt_i32 s15, 1
	v_or_b32_e32 v90, s14, v98
	v_and_b32_e32 v100, 32, v0
	v_lshlrev_b32_e32 v99, 4, v1
	s_cbranch_scc1 .LBB8_7
	s_load_dwordx8 s[4:11], s[0:1], 0x0
	s_load_dwordx2 s[24:25], s[0:1], 0x20
	s_load_dwordx2 s[30:31], s[0:1], 0x80
	s_load_dwordx2 s[48:49], s[0:1], 0x90
	v_and_b32_e32 v34, 7, v1
	v_lshlrev_b32_e32 v34, 4, v34
	v_lshrrev_b32_e32 v35, 3, v1
	s_lshl_b32 s32, s3, 12
	s_add_i32 s33, s32, 0x2000
	s_add_i32 s32, s32, 0xb500
	s_cmp_lt_u32 s3, 2
	s_cselect_b32 s32, s33, s32
	v_lshlrev_b32_e32 v36, 1, v35
	v_and_b32_e32 v36, 7, v36
	v_or_b32_e32 v37, 1, v36
	v_lshlrev_b32_e32 v36, 4, v36
	v_lshlrev_b32_e32 v37, 4, v37
	v_xor_b32_e32 v36, v36, v34
	v_xor_b32_e32 v37, v37, v34
	v_lshl_add_u32 v39, v35, 9, s32
	v_add_u32_e32 v36, v36, v39
	v_add_u32_e32 v37, v37, v39
	v_lshrrev_b32_e32 v38, 1, v98
	v_and_b32_e32 v38, 7, v38
	v_lshrrev_b32_e32 v39, 3, v100
	v_xor_b32_e32 v38, v38, v39
	v_lshlrev_b32_e32 v38, 4, v38
	v_lshl_add_u32 v39, v98, 7, s32
	v_add_u32_e32 v38, v38, v39
	v_lshlrev_b32_e32 v35, 4, v35
	s_mov_b32 s35, 0x1869f
	v_mov_b32_e32 v2, 0
	v_mov_b32_e32 v3, 0
	v_mov_b32_e32 v4, 0
	v_mov_b32_e32 v5, 0
	v_mov_b32_e32 v6, 0
	v_mov_b32_e32 v7, 0
	v_mov_b32_e32 v8, 0
	v_mov_b32_e32 v9, 0
	v_mov_b32_e32 v10, 0
	v_mov_b32_e32 v11, 0
	v_mov_b32_e32 v12, 0
	v_mov_b32_e32 v13, 0
	v_mov_b32_e32 v14, 0
	v_mov_b32_e32 v15, 0
	v_mov_b32_e32 v16, 0
	v_mov_b32_e32 v17, 0
	v_mov_b32_e32 v18, 0
	v_mov_b32_e32 v19, 0
	v_mov_b32_e32 v20, 0
	v_mov_b32_e32 v21, 0
	v_mov_b32_e32 v22, 0
	v_mov_b32_e32 v23, 0
	v_mov_b32_e32 v24, 0
	v_mov_b32_e32 v25, 0
	v_mov_b32_e32 v26, 0
	v_mov_b32_e32 v27, 0
	v_mov_b32_e32 v28, 0
	v_mov_b32_e32 v29, 0
	v_mov_b32_e32 v30, 0
	v_mov_b32_e32 v31, 0
	v_mov_b32_e32 v32, 0
	v_mov_b32_e32 v33, 0
	s_waitcnt vmcnt(0) lgkmcnt(0)
	v_mov_b32_e32 v42, v70
	v_mov_b32_e32 v43, v71
	v_mov_b32_e32 v44, v72
	v_mov_b32_e32 v45, v73
	v_mov_b32_e32 v46, v74
	v_mov_b32_e32 v47, v75
	v_mov_b32_e32 v48, v76
	v_mov_b32_e32 v49, v77
	v_mov_b32_e32 v50, v78
	v_mov_b32_e32 v51, v79
	v_mov_b32_e32 v52, v80
	v_mov_b32_e32 v53, v81
	v_lshlrev_b32_e32 v39, 2, v90
	global_load_dword v40, v39, s[30:31]
	global_load_dword v41, v39, s[30:31] offset:4
	s_lshl_b32 s34, s20, 2
	v_min_u32_e32 v42, s35, v42
	v_min_u32_e32 v46, s35, v46
	v_min_u32_e32 v43, s35, v43
	v_min_u32_e32 v47, s35, v47
	v_min_u32_e32 v44, s35, v44
	v_min_u32_e32 v48, s35, v48
	v_min_u32_e32 v45, s35, v45
	v_min_u32_e32 v49, s35, v49
	v_lshl_or_b32 v42, v42, 7, v34
	v_lshl_or_b32 v46, v46, 7, v34
	v_lshl_or_b32 v43, v43, 7, v34
	v_lshl_or_b32 v47, v47, 7, v34
	v_lshl_or_b32 v44, v44, 7, v34
	v_lshl_or_b32 v48, v48, 7, v34
	v_lshl_or_b32 v45, v45, 7, v34
	v_lshl_or_b32 v49, v49, 7, v34
	global_load_dwordx4 v[70:73], v42, s[24:25]
	global_load_dwordx4 v[74:77], v43, s[24:25]
	global_load_dwordx4 v[78:81], v44, s[24:25]
	global_load_dwordx4 v[82:85], v45, s[24:25]
	global_load_dwordx4 v[86:89], v46, s[10:11]
	global_load_dwordx4 v[90:93], v47, s[10:11]
	global_load_dwordx4 v[94:97], v48, s[10:11]
	global_load_dwordx4 v[102:105], v49, s[10:11]
	s_add_i32 s34, s34, 0x80
	v_add_u32_e32 v39, s34, v35
	global_load_dwordx4 v[42:45], v39, s[4:5]
	global_load_dwordx4 v[46:49], v39, s[6:7]
	v_lshlrev_b32_e32 v39, 1, v34
	ds_read_b128 v[112:115], v39 offset:53248
	ds_read_b128 v[116:119], v39 offset:53760
	ds_read_b128 v[120:123], v39 offset:53504

.Lcu_noclampsd:
	v_lshl_or_b32 v42, v42, 7, v34
	v_lshl_or_b32 v46, v46, 7, v34
	v_lshl_or_b32 v43, v43, 7, v34
	v_lshl_or_b32 v47, v47, 7, v34
	v_lshl_or_b32 v44, v44, 7, v34
	v_lshl_or_b32 v48, v48, 7, v34
	v_lshl_or_b32 v45, v45, 7, v34
	v_lshl_or_b32 v49, v49, 7, v34
	global_load_dwordx4 v[70:73], v42, s[24:25]
	global_load_dwordx4 v[74:77], v43, s[24:25]
	global_load_dwordx4 v[78:81], v44, s[24:25]
	global_load_dwordx4 v[82:85], v45, s[24:25]
	s_lshl_b32 s34, s20, 2
	s_add_i32 s34, s34, 0x80
	v_add_u32_e32 v39, s34, v35
	global_load_dwordx4 v[50:53], v39, s[8:9]
	s_branch .Lcu_skip1
.Lcu_last1:
	v_or_b32_e32 v39, s14, v98
	v_lshlrev_b32_e32 v39, 7, v39
	v_lshl_add_u32 v39, v100, 1, v39
	global_load_dwordx4 v[70:73], v39, s[48:49] offset:48
	global_load_dwordx4 v[74:77], v39, s[48:49] offset:32
	global_load_dwordx4 v[78:81], v39, s[48:49] offset:16
	global_load_dwordx4 v[82:85], v39, s[48:49]

.Lcu_skip2:
	s_nop 9
	v_fma_f32 v110, v67, v112, v69
	v_fma_f32 v111, v67, v113, v69
	v_max_f32_e32 v110, 0, v110
	v_max_f32_e32 v111, 0, v111
	v_cvt_pk_bf16_f32 v106, v110, v111
	v_fma_f32 v110, v67, v114, v69
	v_fma_f32 v111, v67, v115, v69
	v_max_f32_e32 v110, 0, v110
	v_max_f32_e32 v111, 0, v111
	v_cvt_pk_bf16_f32 v107, v110, v111
	v_fma_f32 v110, v67, v116, v69
	v_fma_f32 v111, v67, v117, v69
	v_max_f32_e32 v110, 0, v110
	v_max_f32_e32 v111, 0, v111
	v_cvt_pk_bf16_f32 v108, v110, v111
	v_fma_f32 v110, v67, v118, v69
	v_fma_f32 v111, v67, v119, v69
	v_max_f32_e32 v110, 0, v110
	v_max_f32_e32 v111, 0, v111
	v_cvt_pk_bf16_f32 v109, v110, v111
	s_nop 1
	v_mfma_f32_32x32x16_bf16 v[2:17], v[106:109], v[54:57], v[2:17]
	v_fma_f32 v110, v67, v120, v69
	v_fma_f32 v111, v67, v121, v69
	v_max_f32_e32 v110, 0, v110
	v_max_f32_e32 v111, 0, v111
	v_cvt_pk_bf16_f32 v106, v110, v111
	v_fma_f32 v110, v67, v122, v69
	v_fma_f32 v111, v67, v123, v69
	v_max_f32_e32 v110, 0, v110
	v_max_f32_e32 v111, 0, v111
	v_cvt_pk_bf16_f32 v107, v110, v111
	v_fma_f32 v110, v67, v124, v69
	v_fma_f32 v111, v67, v125, v69
	v_max_f32_e32 v110, 0, v110
	v_max_f32_e32 v111, 0, v111
	v_cvt_pk_bf16_f32 v108, v110, v111
	v_fma_f32 v110, v67, v126, v69
	v_fma_f32 v111, v67, v127, v69
	v_max_f32_e32 v110, 0, v110
	v_max_f32_e32 v111, 0, v111
	v_cvt_pk_bf16_f32 v109, v110, v111
	s_nop 1
	v_mfma_f32_32x32x16_bf16 v[2:17], v[106:109], v[58:61], v[2:17]
	v_lshlrev_b32_e32 v39, 1, v34
	ds_read_b128 v[112:115], v39 offset:53248
	ds_read_b128 v[116:119], v39 offset:53760
	ds_read_b128 v[120:123], v39 offset:53504
	s_add_i32 s20, s20, 32
	s_add_i32 s15, s15, -1
	s_cmp_lg_u32 s15, 0
	s_cbranch_scc1 .Lcu_loop
	s_waitcnt vmcnt(0)
	v_mov_b32_e32 v68, v70
	v_mov_b32_e32 v69, v71
	v_mov_b32_e32 v70, v72
	v_mov_b32_e32 v71, v73
	v_mov_b32_e32 v72, v74
	v_mov_b32_e32 v73, v75
	v_mov_b32_e32 v74, v76
	v_mov_b32_e32 v75, v77
	v_mov_b32_e32 v76, v78
	v_mov_b32_e32 v77, v79
	v_mov_b32_e32 v78, v80
	v_mov_b32_e32 v79, v81
	v_mov_b32_e32 v80, v82
	v_mov_b32_e32 v81, v83
	v_mov_b32_e32 v82, v84
	v_mov_b32_e32 v83, v85
	s_mov_b32 s37, 1
	v_or_b32_e32 v90, s14, v98
	s_branch .LBB8_8

.LBB8_8:
	s_load_dwordx2 s[4:5], s[0:1], 0xa0
	s_load_dwordx2 s[6:7], s[0:1], 0x90
	v_lshlrev_b32_e32 v38, 1, v98
	v_mov_b32_e32 v34, 0
	s_and_b64 vcc, exec, s[16:17]
	v_mov_b32_e32 v35, 0
	v_mov_b32_e32 v36, 0
	v_mov_b32_e32 v37, 0
	s_cbranch_vccz .LBB8_10
	v_ashrrev_i32_e32 v91, 31, v90
	v_lshlrev_b64 v[36:37], 7, v[90:91]
	v_lshlrev_b32_e32 v66, 1, v100
	v_mov_b32_e32 v67, 0
	s_waitcnt lgkmcnt(0)
	v_lshl_add_u64 v[36:37], s[6:7], 0, v[36:37]
	v_lshlrev_b32_e32 v34, 2, v38
	v_lshl_add_u64 v[36:37], v[36:37], 0, v[66:67]
	global_load_dwordx2 v[34:35], v34, s[18:19]
	s_nop 0
	s_cmp_lg_u32 s37, 0
	s_cbranch_scc1 .Lcu_hskip
	global_load_dwordx4 v[68:71], v[36:37], off offset:48
	global_load_dwordx4 v[72:75], v[36:37], off offset:32
	global_load_dwordx4 v[76:79], v[36:37], off offset:16
	global_load_dwordx4 v[80:83], v[36:37], off
.Lcu_hskip:
	v_cvt_pk_f16_f32 v18, v18, v19
	v_cvt_pk_f16_f32 v19, v20, v21
	v_cvt_pk_f16_f32 v20, v22, v23
	v_cvt_pk_f16_f32 v21, v24, v25
	v_cvt_pk_f16_f32 v2, v2, v3
	v_cvt_pk_f16_f32 v3, v4, v5
	v_cvt_pk_f16_f32 v4, v6, v7
	v_cvt_pk_f16_f32 v5, v8, v9
	v_lshlrev_b32_e32 v66, 2, v98
	s_waitcnt vmcnt(0)
	ds_read_b128 v[46:49], v99 offset:16384
	ds_read_b128 v[84:87], v99 offset:17408
	v_mov_b32_e32 v50, v34
	v_mov_b32_e32 v51, v34
	v_mov_b32_e32 v52, v34
	v_mov_b32_e32 v53, v34
	v_mov_b32_e32 v54, v34
	v_mov_b32_e32 v55, v34
	v_mov_b32_e32 v56, v34
	v_mov_b32_e32 v57, v34
	v_mov_b32_e32 v58, v34
	v_mov_b32_e32 v59, v34
	v_mov_b32_e32 v60, v34
	v_mov_b32_e32 v61, v34
	v_mov_b32_e32 v62, v34
	v_mov_b32_e32 v63, v34
	v_mov_b32_e32 v64, v34
	v_mov_b32_e32 v65, v34
	ds_read_b128 v[88:91], v99 offset:20480
	ds_read_b128 v[92:95], v99 offset:21504
	s_waitcnt lgkmcnt(3)
	v_mfma_f32_32x32x16_f16 v[50:65], v[80:83], v[46:49], v[50:65]
	v_mov_b32_e32 v34, v35
	v_mov_b32_e32 v36, v35
	v_mov_b32_e32 v37, v35
	v_mov_b32_e32 v38, v35
	v_mov_b32_e32 v39, v35
	v_mov_b32_e32 v40, v35
	v_mov_b32_e32 v41, v35
	v_mov_b32_e32 v42, v35
	v_mov_b32_e32 v43, v35
	v_mov_b32_e32 v44, v35
	v_mov_b32_e32 v45, v35
	v_mov_b32_e32 v46, v35
	v_mov_b32_e32 v47, v35
	v_mov_b32_e32 v48, v35
	v_mov_b32_e32 v49, v35
	s_waitcnt lgkmcnt(1)
	s_nop 0
	v_mfma_f32_32x32x16_f16 v[34:49], v[80:83], v[88:91], v[34:49]
	ds_read_b128 v[88:91], v99 offset:24576
	ds_read_b128 v[100:103], v99 offset:25600
	s_waitcnt lgkmcnt(1)
	v_mfma_f32_32x32x16_f16 v[50:65], v[80:83], v[88:91], v[50:65]
	ds_read_b128 v[88:91], v99 offset:28672
	ds_read_b128 v[104:107], v99 offset:29696
	s_waitcnt lgkmcnt(1)
	v_mfma_f32_32x32x16_f16 v[34:49], v[80:83], v[88:91], v[34:49]
	v_mfma_f32_32x32x16_f16 v[50:65], v[76:79], v[84:87], v[50:65]
	v_mfma_f32_32x32x16_f16 v[34:49], v[76:79], v[92:95], v[34:49]
	v_mfma_f32_32x32x16_f16 v[50:65], v[76:79], v[100:103], v[50:65]
	s_waitcnt lgkmcnt(0)
	v_mfma_f32_32x32x16_f16 v[34:49], v[76:79], v[104:107], v[34:49]
	ds_read_b128 v[76:79], v99 offset:18432
	ds_read_b128 v[80:83], v99 offset:19456
	s_waitcnt lgkmcnt(1)
	v_mfma_f32_32x32x16_f16 v[50:65], v[72:75], v[76:79], v[50:65]
	ds_read_b128 v[76:79], v99 offset:22528
	ds_read_b128 v[84:87], v99 offset:23552
	s_waitcnt lgkmcnt(1)
	v_mfma_f32_32x32x16_f16 v[34:49], v[72:75], v[76:79], v[34:49]
	ds_read_b128 v[76:79], v99 offset:26624
	ds_read_b128 v[88:91], v99 offset:27648
	s_waitcnt lgkmcnt(1)
	v_mfma_f32_32x32x16_f16 v[50:65], v[72:75], v[76:79], v[50:65]
	ds_read_b128 v[76:79], v99 offset:30720
	ds_read_b128 v[92:95], v99 offset:31744
	s_waitcnt lgkmcnt(1)
	v_mfma_f32_32x32x16_f16 v[34:49], v[72:75], v[76:79], v[34:49]
	v_mfma_f32_32x32x16_f16 v[50:65], v[68:71], v[80:83], v[50:65]
	v_mfma_f32_32x32x16_f16 v[34:49], v[68:71], v[84:87], v[34:49]
	v_mfma_f32_32x32x16_f16 v[50:65], v[68:71], v[88:91], v[50:65]
	s_waitcnt lgkmcnt(0)
	v_mfma_f32_32x32x16_f16 v[34:49], v[68:71], v[92:95], v[34:49]
	ds_read_b128 v[22:25], v99 offset:32768
	ds_read_b128 v[68:71], v99 offset:33792
	s_waitcnt lgkmcnt(1)
	v_mfma_f32_32x32x16_f16 v[50:65], v[18:21], v[22:25], v[50:65]
	s_waitcnt lgkmcnt(0)
	v_mfma_f32_32x32x16_f16 v[34:49], v[18:21], v[68:71], v[34:49]
	ds_read_b128 v[22:25], v99 offset:40960
	ds_read_b128 v[68:71], v99 offset:41984
	s_waitcnt lgkmcnt(1)
	v_mfma_f32_32x32x16_f16 v[50:65], v[18:21], v[22:25], v[50:65]
	v_cvt_pk_f16_f32 v22, v26, v27
	v_cvt_pk_f16_f32 v23, v28, v29
	v_cvt_pk_f16_f32 v24, v30, v31
	v_cvt_pk_f16_f32 v25, v32, v33
	s_waitcnt lgkmcnt(0)
	v_mfma_f32_32x32x16_f16 v[34:49], v[18:21], v[68:71], v[34:49]
	ds_read_b128 v[18:21], v99 offset:34816
	ds_read_b128 v[26:29], v99 offset:35840
	s_waitcnt lgkmcnt(1)
	v_mfma_f32_32x32x16_f16 v[50:65], v[22:25], v[18:21], v[50:65]
	s_waitcnt lgkmcnt(0)
	v_mfma_f32_32x32x16_f16 v[34:49], v[22:25], v[26:29], v[34:49]
	ds_read_b128 v[18:21], v99 offset:43008
	ds_read_b128 v[26:29], v99 offset:44032
	s_waitcnt lgkmcnt(1)
	v_mfma_f32_32x32x16_f16 v[50:65], v[22:25], v[18:21], v[50:65]
	ds_read_b128 v[6:9], v99 offset:36864
	ds_read_b128 v[18:21], v99 offset:37888
	s_waitcnt lgkmcnt(2)
	v_mfma_f32_32x32x16_f16 v[34:49], v[22:25], v[26:29], v[34:49]
	s_waitcnt lgkmcnt(1)
	v_mfma_f32_32x32x16_f16 v[50:65], v[2:5], v[6:9], v[50:65]
	s_waitcnt lgkmcnt(0)
	v_mfma_f32_32x32x16_f16 v[34:49], v[2:5], v[18:21], v[34:49]
	ds_read_b128 v[6:9], v99 offset:45056
	ds_read_b128 v[18:21], v99 offset:46080
	s_waitcnt lgkmcnt(1)
	v_mfma_f32_32x32x16_f16 v[50:65], v[2:5], v[6:9], v[50:65]
	v_cvt_pk_f16_f32 v8, v10, v11
	v_cvt_pk_f16_f32 v9, v12, v13
	v_cvt_pk_f16_f32 v10, v14, v15
	v_cvt_pk_f16_f32 v11, v16, v17
	s_waitcnt lgkmcnt(0)
	v_mfma_f32_32x32x16_f16 v[34:49], v[2:5], v[18:21], v[34:49]
	ds_read_b128 v[2:5], v99 offset:38912
	ds_read_b128 v[12:15], v99 offset:39936
	s_waitcnt lgkmcnt(1)
	v_mfma_f32_32x32x16_f16 v[50:65], v[8:11], v[2:5], v[50:65]
	s_waitcnt lgkmcnt(0)
	v_mfma_f32_32x32x16_f16 v[34:49], v[8:11], v[12:15], v[34:49]
	ds_read_b128 v[2:5], v99 offset:47104
	ds_read_b128 v[12:15], v99 offset:48128
	s_waitcnt lgkmcnt(1)
	v_mfma_f32_32x32x16_f16 v[50:65], v[8:11], v[2:5], v[50:65]
	v_lshrrev_b32_e32 v2, 3, v0
	v_and_or_b32 v6, v2, 4, s14
	v_ashrrev_i32_e32 v7, 31, v6
	v_lshl_add_u64 v[4:5], s[4:5], 0, v[66:67]
	v_or_b32_e32 v16, 16, v6
	v_ashrrev_i32_e32 v17, 31, v16
	v_lshlrev_b64 v[16:17], 7, v[16:17]
	s_waitcnt lgkmcnt(0)
	v_mfma_f32_32x32x16_f16 v[34:49], v[8:11], v[12:15], v[34:49]
	v_lshlrev_b64 v[8:9], 7, v[6:7]
	v_lshl_add_u64 v[8:9], v[4:5], 0, v[8:9]
	v_or_b32_e32 v12, 8, v6
	v_ashrrev_i32_e32 v13, 31, v12
	v_lshlrev_b64 v[12:13], 7, v[12:13]
	v_lshl_add_u64 v[12:13], v[4:5], 0, v[12:13]
	v_or_b32_e32 v14, 10, v6
	s_nop 4
	v_cvt_pk_bf16_f32 v10, v50, v34
	global_store_dword v[8:9], v10, off
	v_or_b32_e32 v8, 1, v6
	v_ashrrev_i32_e32 v9, 31, v8
	v_or_b32_e32 v10, 2, v6
	v_lshlrev_b64 v[8:9], 7, v[8:9]
	v_ashrrev_i32_e32 v11, 31, v10
	v_cvt_pk_bf16_f32 v7, v51, v35
	v_lshl_add_u64 v[8:9], v[4:5], 0, v[8:9]
	v_lshlrev_b64 v[10:11], 7, v[10:11]
	global_store_dword v[8:9], v7, off
	v_cvt_pk_bf16_f32 v7, v52, v36
	v_lshl_add_u64 v[10:11], v[4:5], 0, v[10:11]
	global_store_dword v[10:11], v7, off
	v_or_b32_e32 v10, 3, v6
	v_ashrrev_i32_e32 v11, 31, v10
	v_lshlrev_b64 v[10:11], 7, v[10:11]
	v_cvt_pk_bf16_f32 v7, v53, v37
	v_lshl_add_u64 v[10:11], v[4:5], 0, v[10:11]
	global_store_dword v[10:11], v7, off
	v_cvt_pk_bf16_f32 v7, v54, v38
	global_store_dword v[12:13], v7, off
	v_or_b32_e32 v12, 9, v6
	v_ashrrev_i32_e32 v13, 31, v12
	v_lshlrev_b64 v[12:13], 7, v[12:13]
	v_ashrrev_i32_e32 v15, 31, v14
	v_cvt_pk_bf16_f32 v7, v55, v39
	v_lshl_add_u64 v[12:13], v[4:5], 0, v[12:13]
	v_lshlrev_b64 v[14:15], 7, v[14:15]
	global_store_dword v[12:13], v7, off
	v_cvt_pk_bf16_f32 v7, v56, v40
	v_lshl_add_u64 v[14:15], v[4:5], 0, v[14:15]
	global_store_dword v[14:15], v7, off
	v_or_b32_e32 v14, 11, v6
	v_ashrrev_i32_e32 v15, 31, v14
	v_lshlrev_b64 v[14:15], 7, v[14:15]
	v_cvt_pk_bf16_f32 v7, v57, v41
	v_lshl_add_u64 v[14:15], v[4:5], 0, v[14:15]
	global_store_dword v[14:15], v7, off
	v_cvt_pk_bf16_f32 v7, v58, v42
	v_lshl_add_u64 v[16:17], v[4:5], 0, v[16:17]
	global_store_dword v[16:17], v7, off
	v_or_b32_e32 v16, 17, v6
	v_ashrrev_i32_e32 v17, 31, v16
	v_or_b32_e32 v18, 18, v6
	v_lshlrev_b64 v[16:17], 7, v[16:17]
	v_ashrrev_i32_e32 v19, 31, v18
	v_cvt_pk_bf16_f32 v7, v59, v43
	v_lshl_add_u64 v[16:17], v[4:5], 0, v[16:17]
	v_lshlrev_b64 v[18:19], 7, v[18:19]
	global_store_dword v[16:17], v7, off
	v_cvt_pk_bf16_f32 v7, v60, v44
	v_lshl_add_u64 v[18:19], v[4:5], 0, v[18:19]
	global_store_dword v[18:19], v7, off
	v_or_b32_e32 v18, 19, v6
	v_ashrrev_i32_e32 v19, 31, v18
	v_or_b32_e32 v20, 24, v6
	v_lshlrev_b64 v[18:19], 7, v[18:19]
	v_ashrrev_i32_e32 v21, 31, v20
	v_cvt_pk_bf16_f32 v7, v61, v45
	v_lshl_add_u64 v[18:19], v[4:5], 0, v[18:19]
	v_lshlrev_b64 v[20:21], 7, v[20:21]
	global_store_dword v[18:19], v7, off
	v_cvt_pk_bf16_f32 v7, v62, v46
	v_lshl_add_u64 v[20:21], v[4:5], 0, v[20:21]
	global_store_dword v[20:21], v7, off
	v_or_b32_e32 v20, 25, v6
	v_ashrrev_i32_e32 v21, 31, v20
	v_or_b32_e32 v22, 26, v6
	v_lshlrev_b64 v[20:21], 7, v[20:21]
	v_ashrrev_i32_e32 v23, 31, v22
	v_cvt_pk_bf16_f32 v7, v63, v47
	v_lshl_add_u64 v[20:21], v[4:5], 0, v[20:21]
	v_lshlrev_b64 v[22:23], 7, v[22:23]
	global_store_dword v[20:21], v7, off
	v_cvt_pk_bf16_f32 v7, v64, v48
	v_lshl_add_u64 v[22:23], v[4:5], 0, v[22:23]
	v_or_b32_e32 v6, 27, v6
	global_store_dword v[22:23], v7, off
	v_ashrrev_i32_e32 v7, 31, v6
	v_lshlrev_b64 v[6:7], 7, v[6:7]
	v_mov_b32_e32 v2, v50
	v_mov_b32_e32 v3, v34
	v_cvt_pk_bf16_f32 v22, v65, v49
	v_lshl_add_u64 v[4:5], v[4:5], 0, v[6:7]
	v_mov_b32_e32 v34, v51
	global_store_dword v[4:5], v22, off
	v_pk_add_f32 v[4:5], v[2:3], 0 op_sel_hi:[1,0]
	v_pk_fma_f32 v[2:3], v[2:3], v[2:3], 0 op_sel_hi:[1,1,0]
	v_mov_b32_e32 v8, v52
	v_mov_b32_e32 v9, v36
	v_pk_add_f32 v[4:5], v[4:5], v[34:35]
	v_pk_fma_f32 v[2:3], v[34:35], v[34:35], v[2:3]
	v_mov_b32_e32 v36, v53
	v_pk_add_f32 v[4:5], v[4:5], v[8:9]
	v_pk_fma_f32 v[2:3], v[8:9], v[8:9], v[2:3]
	v_mov_b32_e32 v10, v54
	v_mov_b32_e32 v11, v38
	v_pk_add_f32 v[4:5], v[4:5], v[36:37]
	v_pk_fma_f32 v[2:3], v[36:37], v[36:37], v[2:3]
	v_mov_b32_e32 v38, v55
	v_pk_add_f32 v[4:5], v[4:5], v[10:11]
	v_pk_fma_f32 v[2:3], v[10:11], v[10:11], v[2:3]
	v_mov_b32_e32 v12, v56
	v_mov_b32_e32 v13, v40
	v_pk_add_f32 v[4:5], v[4:5], v[38:39]
	v_pk_fma_f32 v[2:3], v[38:39], v[38:39], v[2:3]
	v_mov_b32_e32 v40, v57
	v_pk_add_f32 v[4:5], v[4:5], v[12:13]
	v_pk_fma_f32 v[2:3], v[12:13], v[12:13], v[2:3]
	v_mov_b32_e32 v14, v58
	v_mov_b32_e32 v15, v42
	v_pk_add_f32 v[4:5], v[4:5], v[40:41]
	v_pk_fma_f32 v[2:3], v[40:41], v[40:41], v[2:3]
	v_mov_b32_e32 v42, v59
	v_pk_add_f32 v[4:5], v[4:5], v[14:15]
	v_pk_fma_f32 v[2:3], v[14:15], v[14:15], v[2:3]
	v_mov_b32_e32 v16, v60
	v_mov_b32_e32 v17, v44
	v_pk_add_f32 v[4:5], v[4:5], v[42:43]
	v_pk_fma_f32 v[2:3], v[42:43], v[42:43], v[2:3]
	v_mov_b32_e32 v44, v61
	v_pk_add_f32 v[4:5], v[4:5], v[16:17]
	v_pk_fma_f32 v[2:3], v[16:17], v[16:17], v[2:3]
	v_mov_b32_e32 v18, v62
	v_mov_b32_e32 v19, v46
	v_pk_add_f32 v[4:5], v[4:5], v[44:45]
	v_pk_fma_f32 v[2:3], v[44:45], v[44:45], v[2:3]
	v_mov_b32_e32 v46, v63
	v_pk_add_f32 v[4:5], v[4:5], v[18:19]
	v_pk_fma_f32 v[2:3], v[18:19], v[18:19], v[2:3]
	v_mov_b32_e32 v20, v64
	v_mov_b32_e32 v21, v48
	v_pk_add_f32 v[4:5], v[4:5], v[46:47]
	v_pk_fma_f32 v[2:3], v[46:47], v[46:47], v[2:3]
	v_mov_b32_e32 v48, v65
	v_pk_add_f32 v[4:5], v[4:5], v[20:21]
	v_pk_fma_f32 v[2:3], v[20:21], v[20:21], v[2:3]
	v_pk_add_f32 v[34:35], v[4:5], v[48:49]
	v_pk_fma_f32 v[36:37], v[48:49], v[48:49], v[2:3]
